# E7: E5 + G1 gather row-offset VALU moved from the head of the MFMA segment to before the barrier
# speedup vs baseline: 1.0111x; 1.0027x over previous
.LBB0_1214:
	ds_read_b128 v[70:73], v190
	ds_read_b128 v[74:77], v190 offset:1024
	ds_read_b128 v[78:81], v190 offset:2048
	ds_read_b128 v[82:85], v190 offset:3072
	ds_read_b128 v[94:97], v191
	ds_read_b128 v[98:101], v191 offset:1024
	ds_read_b128 v[102:105], v191 offset:2048
	ds_read_b128 v[106:109], v191 offset:3072
	s_add_u32 s44, s42, 0x100
	s_addc_u32 s45, s43, 0
	s_add_u32 s48, s35, s42
	s_addc_u32 s49, s37, s43
	s_cmp_eq_u32 s39, 12
	s_cselect_b64 vcc, -1, 0
	s_and_b64 s[46:47], vcc, exec
	s_cselect_b32 s73, 0, s44
	s_cselect_b32 s72, 0, s45
	s_cselect_b32 s46, s0, s48
	s_cselect_b32 s47, s1, s49
	s_add_u32 s48, s14, s73
	s_addc_u32 s49, s15, s72
	s_add_i32 m0, s11, 0xc000
	s_add_u32 s42, s24, s42
	s_addc_u32 s43, s25, s43
	ds_read_b128 v[176:179], v192
	ds_read_b128 v[180:183], v192 offset:1024
	ds_read_b128 v[194:197], v192 offset:2048
	ds_read_b128 v[198:201], v192 offset:3072
	ds_read_b128 v[202:205], v192 offset:4096
	ds_read_b128 v[206:209], v192 offset:5120
	ds_read_b128 v[210:213], v192 offset:6144
	ds_read_b128 v[214:217], v192 offset:7168
	global_load_lds_dwordx4 v187, s[42:43]
	s_add_i32 m0, s11, 0xe000
	v_mov_b32_e32 v0, v172
	global_load_lds_dwordx4 v186, s[42:43]
	v_mov_b32_e32 v169, v173
	v_lshlrev_b32_e32 v184, 11, v0
	v_lshlrev_b32_e32 v185, 11, v169
	v_bfe_u32 v0, v0, 16, 16
	v_bfe_u32 v169, v169, 16, 16
	v_and_b32_e32 v184, 0x7fff800, v184
	v_and_b32_e32 v185, 0x7fff800, v185
	v_lshl_add_u32 v0, v0, 11, v175
	v_lshl_add_u32 v169, v169, 11, v175
	v_add_u32_e32 v184, v184, v175
	v_add_u32_e32 v185, v185, v175
	v_cndmask_b32_e32 v168, v168, v0, vcc
	v_cndmask_b32_e32 v186, v186, v169, vcc
	v_cndmask_b32_e32 v170, v170, v184, vcc
	v_cndmask_b32_e32 v187, v187, v185, vcc
	s_waitcnt vmcnt(8)
	s_waitcnt lgkmcnt(0)
	s_barrier
	s_setprio 1
	s_waitcnt lgkmcnt(0)
	v_mfma_i32_16x16x64_i8 v[158:161], v[70:73], v[176:179], v[158:161]
	v_mfma_i32_16x16x64_i8 v[150:153], v[78:81], v[176:179], v[150:153]
	v_mfma_i32_16x16x64_i8 v[142:145], v[70:73], v[194:197], v[142:145]
	v_mfma_i32_16x16x64_i8 v[134:137], v[78:81], v[194:197], v[134:137]
	v_mfma_i32_16x16x64_i8 v[126:129], v[70:73], v[202:205], v[126:129]
	v_mfma_i32_16x16x64_i8 v[118:121], v[78:81], v[202:205], v[118:121]
	v_mfma_i32_16x16x64_i8 v[110:113], v[70:73], v[210:213], v[110:113]
	v_mfma_i32_16x16x64_i8 v[86:89], v[78:81], v[210:213], v[86:89]
	v_mfma_i32_16x16x64_i8 v[158:161], v[74:77], v[180:183], v[158:161]
	v_mfma_i32_16x16x64_i8 v[150:153], v[82:85], v[180:183], v[150:153]
	v_mfma_i32_16x16x64_i8 v[142:145], v[74:77], v[198:201], v[142:145]
	v_mfma_i32_16x16x64_i8 v[134:137], v[82:85], v[198:201], v[134:137]
	v_mfma_i32_16x16x64_i8 v[126:129], v[74:77], v[206:209], v[126:129]
	v_mfma_i32_16x16x64_i8 v[118:121], v[82:85], v[206:209], v[118:121]
	v_mfma_i32_16x16x64_i8 v[110:113], v[74:77], v[214:217], v[110:113]
	v_mfma_i32_16x16x64_i8 v[86:89], v[82:85], v[214:217], v[86:89]
	s_setprio 0
	s_setprio 1
	v_mfma_i32_16x16x64_i8 v[154:157], v[94:97], v[176:179], v[154:157]
	v_mfma_i32_16x16x64_i8 v[146:149], v[102:105], v[176:179], v[146:149]
	v_mfma_i32_16x16x64_i8 v[138:141], v[94:97], v[194:197], v[138:141]
	v_mfma_i32_16x16x64_i8 v[130:133], v[102:105], v[194:197], v[130:133]
	v_mfma_i32_16x16x64_i8 v[122:125], v[94:97], v[202:205], v[122:125]
	v_mfma_i32_16x16x64_i8 v[114:117], v[102:105], v[202:205], v[114:117]
	v_mfma_i32_16x16x64_i8 v[90:93], v[94:97], v[210:213], v[90:93]
	v_mfma_i32_16x16x64_i8 v[66:69], v[102:105], v[210:213], v[66:69]
	v_mfma_i32_16x16x64_i8 v[154:157], v[98:101], v[180:183], v[154:157]
	v_mfma_i32_16x16x64_i8 v[146:149], v[106:109], v[180:183], v[146:149]
	v_mfma_i32_16x16x64_i8 v[138:141], v[98:101], v[198:201], v[138:141]
	v_mfma_i32_16x16x64_i8 v[130:133], v[106:109], v[198:201], v[130:133]
	v_mfma_i32_16x16x64_i8 v[122:125], v[98:101], v[206:209], v[122:125]
	v_mfma_i32_16x16x64_i8 v[114:117], v[106:109], v[206:209], v[114:117]
	v_mfma_i32_16x16x64_i8 v[90:93], v[98:101], v[214:217], v[90:93]
	v_mfma_i32_16x16x64_i8 v[66:69], v[106:109], v[214:217], v[66:69]
	s_setprio 0
	s_barrier
	s_add_i32 s42, s67, s57
	v_lshl_add_u64 v[184:185], s[46:47], 0, v[164:165]
	s_mov_b32 m0, s42
	ds_read_b128 v[176:179], v192 offset:16384
	ds_read_b128 v[180:183], v192 offset:17408
	ds_read_b128 v[194:197], v192 offset:18432
	ds_read_b128 v[198:201], v192 offset:19456
	ds_read_b128 v[202:205], v192 offset:20480
	ds_read_b128 v[206:209], v192 offset:21504
	ds_read_b128 v[210:213], v192 offset:22528
	ds_read_b128 v[214:217], v192 offset:23552
	global_load_lds_dwordx4 v[184:185], off
	s_add_i32 m0, s42, 0x2000
	s_add_u32 s42, s46, 0x40000
	v_lshl_add_u64 v[218:219], s[46:47], 0, v[166:167]
	s_addc_u32 s43, s47, 0
	s_add_i32 s72, s68, s57
	global_load_lds_dwordx4 v[218:219], off
	v_lshl_add_u64 v[220:221], s[42:43], 0, v[164:165]
	s_mov_b32 m0, s72
	v_mov_b32_e32 v169, v171
	global_load_lds_dwordx4 v[220:221], off
	v_lshl_add_u64 v[220:221], s[42:43], 0, v[166:167]
	s_add_i32 m0, s72, 0x2000
	v_lshl_add_u64 v[222:223], s[48:49], 0, v[168:169]
	global_load_lds_dwordx4 v[220:221], off
	s_mov_b32 m0, s11
	v_lshl_add_u64 v[220:221], s[48:49], 0, v[170:171]
	global_load_lds_dwordx4 v170, s[48:49]
	s_mov_b32 m0, s58
	s_nop 0
	global_load_lds_dwordx4 v168, s[48:49]
	s_waitcnt vmcnt(8)
	s_waitcnt lgkmcnt(0)
	s_barrier
	s_setprio 1
	s_waitcnt lgkmcnt(0)
	v_mfma_i32_16x16x64_i8 v[62:65], v[70:73], v[176:179], v[62:65]
	v_mfma_i32_16x16x64_i8 v[54:57], v[78:81], v[176:179], v[54:57]
	v_mfma_i32_16x16x64_i8 v[46:49], v[70:73], v[194:197], v[46:49]
	v_mfma_i32_16x16x64_i8 v[38:41], v[78:81], v[194:197], v[38:41]
	v_mfma_i32_16x16x64_i8 v[30:33], v[70:73], v[202:205], v[30:33]
	v_mfma_i32_16x16x64_i8 v[22:25], v[78:81], v[202:205], v[22:25]
	v_mfma_i32_16x16x64_i8 v[14:17], v[70:73], v[210:213], v[14:17]
	v_mfma_i32_16x16x64_i8 v[6:9], v[78:81], v[210:213], v[6:9]
	v_mfma_i32_16x16x64_i8 v[62:65], v[74:77], v[180:183], v[62:65]
	v_mfma_i32_16x16x64_i8 v[54:57], v[82:85], v[180:183], v[54:57]
	v_mfma_i32_16x16x64_i8 v[46:49], v[74:77], v[198:201], v[46:49]
	v_mfma_i32_16x16x64_i8 v[38:41], v[82:85], v[198:201], v[38:41]
	v_mfma_i32_16x16x64_i8 v[30:33], v[74:77], v[206:209], v[30:33]
	v_mfma_i32_16x16x64_i8 v[22:25], v[82:85], v[206:209], v[22:25]
	v_mfma_i32_16x16x64_i8 v[14:17], v[74:77], v[214:217], v[14:17]
	v_mfma_i32_16x16x64_i8 v[6:9], v[82:85], v[214:217], v[6:9]
	s_setprio 0
	s_setprio 1
	v_mfma_i32_16x16x64_i8 v[58:61], v[94:97], v[176:179], v[58:61]
	v_mfma_i32_16x16x64_i8 v[50:53], v[102:105], v[176:179], v[50:53]
	v_mfma_i32_16x16x64_i8 v[42:45], v[94:97], v[194:197], v[42:45]
	v_mfma_i32_16x16x64_i8 v[34:37], v[102:105], v[194:197], v[34:37]
	v_mfma_i32_16x16x64_i8 v[26:29], v[94:97], v[202:205], v[26:29]
	v_mfma_i32_16x16x64_i8 v[18:21], v[102:105], v[202:205], v[18:21]
	v_mfma_i32_16x16x64_i8 v[10:13], v[94:97], v[210:213], v[10:13]
	v_mfma_i32_16x16x64_i8 v[2:5], v[102:105], v[210:213], v[2:5]
	v_mfma_i32_16x16x64_i8 v[58:61], v[98:101], v[180:183], v[58:61]
	v_mfma_i32_16x16x64_i8 v[50:53], v[106:109], v[180:183], v[50:53]
	v_mfma_i32_16x16x64_i8 v[42:45], v[98:101], v[198:201], v[42:45]
	v_mfma_i32_16x16x64_i8 v[34:37], v[106:109], v[198:201], v[34:37]
	v_mfma_i32_16x16x64_i8 v[26:29], v[98:101], v[206:209], v[26:29]
	v_mfma_i32_16x16x64_i8 v[18:21], v[106:109], v[206:209], v[18:21]
	v_mfma_i32_16x16x64_i8 v[10:13], v[98:101], v[214:217], v[10:13]
	v_mfma_i32_16x16x64_i8 v[2:5], v[106:109], v[214:217], v[2:5]
	s_setprio 0
	s_barrier
	s_add_i32 s42, 0, 0x18000
	v_add_u32_e32 v0, s42, v189
	s_add_i32 s72, 0, 0x1c000
	ds_read_b128 v[70:73], v0
	ds_read_b128 v[74:77], v0 offset:1024
	ds_read_b128 v[78:81], v0 offset:2048
	ds_read_b128 v[82:85], v0 offset:3072
	v_add_u32_e32 v0, s72, v189
	ds_read_b128 v[94:97], v0
	ds_read_b128 v[98:101], v0 offset:1024
	ds_read_b128 v[102:105], v0 offset:2048
	ds_read_b128 v[106:109], v0 offset:3072
	s_mov_b32 m0, s59
	ds_read_b128 v[176:179], v192 offset:32768
	ds_read_b128 v[180:183], v192 offset:33792
	ds_read_b128 v[194:197], v192 offset:34816
	ds_read_b128 v[198:201], v192 offset:35840
	ds_read_b128 v[202:205], v192 offset:36864
	ds_read_b128 v[206:209], v192 offset:37888
	ds_read_b128 v[210:213], v192 offset:38912
	ds_read_b128 v[214:217], v192 offset:39936
	global_load_lds_dwordx4 v187, s[48:49]
	s_mov_b32 m0, s60
	s_nop 0
	global_load_lds_dwordx4 v186, s[48:49]
	s_waitcnt vmcnt(8)
	s_waitcnt lgkmcnt(0)
	s_barrier
	s_setprio 1
	s_waitcnt lgkmcnt(0)
	v_mfma_i32_16x16x64_i8 v[158:161], v[70:73], v[176:179], v[158:161]
	v_mfma_i32_16x16x64_i8 v[150:153], v[78:81], v[176:179], v[150:153]
	v_mfma_i32_16x16x64_i8 v[142:145], v[70:73], v[194:197], v[142:145]
	v_mfma_i32_16x16x64_i8 v[134:137], v[78:81], v[194:197], v[134:137]
	v_mfma_i32_16x16x64_i8 v[126:129], v[70:73], v[202:205], v[126:129]
	v_mfma_i32_16x16x64_i8 v[118:121], v[78:81], v[202:205], v[118:121]
	v_mfma_i32_16x16x64_i8 v[110:113], v[70:73], v[210:213], v[110:113]
	v_mfma_i32_16x16x64_i8 v[86:89], v[78:81], v[210:213], v[86:89]
	v_mfma_i32_16x16x64_i8 v[158:161], v[74:77], v[180:183], v[158:161]
	v_mfma_i32_16x16x64_i8 v[150:153], v[82:85], v[180:183], v[150:153]
	v_mfma_i32_16x16x64_i8 v[142:145], v[74:77], v[198:201], v[142:145]
	v_mfma_i32_16x16x64_i8 v[134:137], v[82:85], v[198:201], v[134:137]
	v_mfma_i32_16x16x64_i8 v[126:129], v[74:77], v[206:209], v[126:129]
	v_mfma_i32_16x16x64_i8 v[118:121], v[82:85], v[206:209], v[118:121]
	v_mfma_i32_16x16x64_i8 v[110:113], v[74:77], v[214:217], v[110:113]
	v_mfma_i32_16x16x64_i8 v[86:89], v[82:85], v[214:217], v[86:89]
	s_setprio 0
	s_setprio 1
	v_mfma_i32_16x16x64_i8 v[154:157], v[94:97], v[176:179], v[154:157]
	v_mfma_i32_16x16x64_i8 v[146:149], v[102:105], v[176:179], v[146:149]
	v_mfma_i32_16x16x64_i8 v[138:141], v[94:97], v[194:197], v[138:141]
	v_mfma_i32_16x16x64_i8 v[130:133], v[102:105], v[194:197], v[130:133]
	v_mfma_i32_16x16x64_i8 v[122:125], v[94:97], v[202:205], v[122:125]
	v_mfma_i32_16x16x64_i8 v[114:117], v[102:105], v[202:205], v[114:117]
	v_mfma_i32_16x16x64_i8 v[90:93], v[94:97], v[210:213], v[90:93]
	v_mfma_i32_16x16x64_i8 v[66:69], v[102:105], v[210:213], v[66:69]
	v_mfma_i32_16x16x64_i8 v[154:157], v[98:101], v[180:183], v[154:157]
	v_mfma_i32_16x16x64_i8 v[146:149], v[106:109], v[180:183], v[146:149]
	v_mfma_i32_16x16x64_i8 v[138:141], v[98:101], v[198:201], v[138:141]
	v_mfma_i32_16x16x64_i8 v[130:133], v[106:109], v[198:201], v[130:133]
	v_mfma_i32_16x16x64_i8 v[122:125], v[98:101], v[206:209], v[122:125]
	v_mfma_i32_16x16x64_i8 v[114:117], v[106:109], v[206:209], v[114:117]
	v_mfma_i32_16x16x64_i8 v[90:93], v[98:101], v[214:217], v[90:93]
	v_mfma_i32_16x16x64_i8 v[66:69], v[106:109], v[214:217], v[66:69]
	s_setprio 0
	s_barrier
	s_add_i32 s42, s42, s57
	v_lshl_add_u64 v[184:185], v[184:185], 0, s[22:23]
	s_mov_b32 m0, s42
	ds_read_b128 v[176:179], v192 offset:49152
	ds_read_b128 v[180:183], v192 offset:50176
	ds_read_b128 v[194:197], v192 offset:51200
	ds_read_b128 v[198:201], v192 offset:52224
	ds_read_b128 v[202:205], v192 offset:53248
	ds_read_b128 v[206:209], v192 offset:54272
	ds_read_b128 v[210:213], v192 offset:55296
	ds_read_b128 v[214:217], v192 offset:56320
	global_load_lds_dwordx4 v[184:185], off
	s_add_i32 m0, s42, 0x2000
	s_add_u32 s42, s46, 0x40080
	v_lshl_add_u64 v[184:185], v[218:219], 0, s[22:23]
	s_addc_u32 s43, s47, 0
	s_add_i32 s46, s72, s57
	global_load_lds_dwordx4 v[184:185], off
	v_lshl_add_u64 v[184:185], s[42:43], 0, v[164:165]
	s_mov_b32 m0, s46
	s_nop 0
	global_load_lds_dwordx4 v[184:185], off
	v_lshl_add_u64 v[184:185], s[42:43], 0, v[166:167]
	s_add_i32 m0, s46, 0x2000
	s_nop 0
	global_load_lds_dwordx4 v[184:185], off
	v_lshl_add_u64 v[184:185], v[220:221], 0, s[22:23]
	s_mov_b32 m0, s63
	s_nop 0
	global_load_lds_dwordx4 v[184:185], off
	v_lshl_add_u64 v[184:185], v[222:223], 0, s[22:23]
	s_mov_b32 m0, s64
	s_nop 0
	global_load_lds_dwordx4 v[184:185], off
	s_waitcnt vmcnt(8)
	s_waitcnt lgkmcnt(0)
	s_barrier
	s_setprio 1
	s_waitcnt lgkmcnt(0)
	v_mfma_i32_16x16x64_i8 v[62:65], v[70:73], v[176:179], v[62:65]
	v_mfma_i32_16x16x64_i8 v[54:57], v[78:81], v[176:179], v[54:57]
	v_mfma_i32_16x16x64_i8 v[46:49], v[70:73], v[194:197], v[46:49]
	v_mfma_i32_16x16x64_i8 v[38:41], v[78:81], v[194:197], v[38:41]
	v_mfma_i32_16x16x64_i8 v[30:33], v[70:73], v[202:205], v[30:33]
	v_mfma_i32_16x16x64_i8 v[22:25], v[78:81], v[202:205], v[22:25]
	v_mfma_i32_16x16x64_i8 v[14:17], v[70:73], v[210:213], v[14:17]
	v_mfma_i32_16x16x64_i8 v[6:9], v[78:81], v[210:213], v[6:9]
	v_mfma_i32_16x16x64_i8 v[62:65], v[74:77], v[180:183], v[62:65]
	v_mfma_i32_16x16x64_i8 v[54:57], v[82:85], v[180:183], v[54:57]
	v_mfma_i32_16x16x64_i8 v[46:49], v[74:77], v[198:201], v[46:49]
	v_mfma_i32_16x16x64_i8 v[38:41], v[82:85], v[198:201], v[38:41]
	v_mfma_i32_16x16x64_i8 v[30:33], v[74:77], v[206:209], v[30:33]
	v_mfma_i32_16x16x64_i8 v[22:25], v[82:85], v[206:209], v[22:25]
	v_mfma_i32_16x16x64_i8 v[14:17], v[74:77], v[214:217], v[14:17]
	v_mfma_i32_16x16x64_i8 v[6:9], v[82:85], v[214:217], v[6:9]
	s_setprio 0
	s_setprio 1
	v_mfma_i32_16x16x64_i8 v[58:61], v[94:97], v[176:179], v[58:61]
	v_mfma_i32_16x16x64_i8 v[50:53], v[102:105], v[176:179], v[50:53]
	v_mfma_i32_16x16x64_i8 v[42:45], v[94:97], v[194:197], v[42:45]
	v_mfma_i32_16x16x64_i8 v[34:37], v[102:105], v[194:197], v[34:37]
	v_mfma_i32_16x16x64_i8 v[26:29], v[94:97], v[202:205], v[26:29]
	v_mfma_i32_16x16x64_i8 v[18:21], v[102:105], v[202:205], v[18:21]
	v_mfma_i32_16x16x64_i8 v[10:13], v[94:97], v[210:213], v[10:13]
	v_mfma_i32_16x16x64_i8 v[2:5], v[102:105], v[210:213], v[2:5]
	v_mfma_i32_16x16x64_i8 v[58:61], v[98:101], v[180:183], v[58:61]
	v_mfma_i32_16x16x64_i8 v[50:53], v[106:109], v[180:183], v[50:53]
	v_mfma_i32_16x16x64_i8 v[42:45], v[98:101], v[198:201], v[42:45]
	v_mfma_i32_16x16x64_i8 v[34:37], v[106:109], v[198:201], v[34:37]
	v_mfma_i32_16x16x64_i8 v[26:29], v[98:101], v[206:209], v[26:29]
	v_mfma_i32_16x16x64_i8 v[18:21], v[106:109], v[206:209], v[18:21]
	v_mfma_i32_16x16x64_i8 v[10:13], v[98:101], v[214:217], v[10:13]
	v_mfma_i32_16x16x64_i8 v[2:5], v[106:109], v[214:217], v[2:5]
	s_setprio 0
	s_barrier
	s_add_i32 s39, s39, 2
	s_cmp_gt_u32 s39, 13
	s_mov_b64 s[42:43], s[44:45]
	s_cbranch_scc0 .LBB0_1214
	s_and_b64 vcc, exec, s[26:27]
	s_cbranch_vccz .LBB0_1217
	s_barrier
